# static priority for waves 4-7 during phase 4 only (MLA attention)
# baseline (speedup 1.0000x reference)
.LBB0_796:
	s_andn2_b64 vcc, exec, s[4:5]
	s_cbranch_vccnz .LBB0_902
	v_cmp_lt_u32_e32 vcc, 255, v0
	s_cbranch_vccz .Lp4prio_skip
	s_setprio 1
.Lp4prio_skip:
	v_readlane_b32 s8, v252, 2
	v_mov_b32_e32 v133, v0
	s_mov_b64 s[4:5], 0
	v_readlane_b32 s10, v252, 4
	v_readlane_b32 s11, v252, 5
	s_add_u32 s10, s10, s4
	v_readfirstlane_b32 s6, v133
	s_addc_u32 s11, s11, s5
	s_cmp_gt_u32 s6, 63
	v_readlane_b32 s6, v253, 28
	s_cselect_b64 s[4:5], -1, 0
	v_readlane_b32 s7, v253, 29
	s_or_b64 s[4:5], s[4:5], s[6:7]
	s_and_b64 vcc, exec, s[4:5]
	v_readlane_b32 s9, v252, 3
	s_cbranch_vccnz .LBB0_802
	s_waitcnt lgkmcnt(0)
	v_bfe_u32 v7, v133, 5, 1
	v_readlane_b32 s4, v252, 2
	s_waitcnt lgkmcnt(0)
	v_lshlrev_b32_e32 v4, 4, v7
	v_mov_b32_e32 v5, v3
	v_readlane_b32 s5, v252, 3
	v_and_b32_e32 v6, 63, v133
	v_and_b32_e32 v9, 64, v250
	v_lshl_add_u64 v[134:135], s[4:5], 0, v[4:5]
	v_readlane_b32 s4, v253, 24
	v_readlane_b32 s5, v253, 25
	v_lshlrev_b32_e32 v8, 6, v6
	v_cmp_gt_u32_e32 vcc, 32, v6
	v_xor_b32_e32 v6, 32, v250
	v_add_u32_e32 v9, 64, v9
	v_lshl_add_u64 v[136:137], s[4:5], 0, v[4:5]
	v_readlane_b32 s4, v253, 22
	v_lshlrev_b32_e32 v2, 3, v7
	v_cmp_lt_i32_e64 s[38:39], v6, v9
	v_readlane_b32 s5, v253, 23
	v_lshl_add_u64 v[4:5], s[10:11], 0, v[2:3]
	v_cndmask_b32_e64 v6, v250, v6, s[38:39]
	v_lshl_add_u64 v[138:139], s[4:5], 0, v[2:3]
	s_mov_b64 s[4:5], 0x1d300000
	s_add_u32 s12, s10, 0x1d280000
	v_and_b32_e32 v132, 0x7c0, v8
	v_lshlrev_b32_e32 v166, 2, v6
	v_or_b32_e32 v6, 0x800, v8
	v_lshlrev_b32_e32 v8, 2, v7
	v_lshl_add_u64 v[140:141], v[4:5], 0, s[4:5]
	v_readlane_b32 s4, v254, 61
	s_addc_u32 s13, s11, 0
	v_lshlrev_b32_e32 v142, 1, v6
	v_lshlrev_b32_e32 v144, 1, v8
	s_mov_b32 s16, s4
	v_readlane_b32 s6, v252, 4
	v_readlane_b32 s7, v252, 5
	v_readlane_b32 s5, v254, 62

.LBB0_902:
	s_setprio 0
	s_cmp_le_i32 s88, s22
	s_cselect_b64 s[4:5], -1, 0
	s_cmp_lt_i32 s22, s89
	s_cselect_b64 s[6:7], -1, 0
	s_and_b64 s[6:7], s[4:5], s[6:7]
	s_mov_b64 s[4:5], -1
	s_and_b64 vcc, exec, s[6:7]
	s_cbranch_vccnz .LBB0_904
	s_add_i32 s22, s74, 6
	s_mov_b64 s[4:5], 0
